# baseline (speedup 1.0000x reference)
.Lno_pre:
	s_nop 15
	s_nop 3
	v_cvt_pk_f16_f32 v38, v64, v65
	v_cvt_pk_f16_f32 v39, v66, v67
	v_and_b32 v36, s35, v38
	v_and_b32 v37, s35, v39
	v_pk_fma_f16 v238, v36, s42, v227
	v_pk_fma_f16 v239, v37, s42, v227
	v_pk_fma_f16 v238, v238, v36, s43
	v_pk_fma_f16 v239, v239, v37, s43
	s_nop 0
	v_pk_mul_f16 v238, v238, v36
	v_pk_mul_f16 v239, v239, v37
	v_exp_f16_sdwa v238, v238 dst_sel:WORD_0 dst_unused:UNUSED_PRESERVE src0_sel:WORD_0
	v_exp_f16_sdwa v239, v239 dst_sel:WORD_0 dst_unused:UNUSED_PRESERVE src0_sel:WORD_0
	v_exp_f16_sdwa v238, v238 dst_sel:WORD_1 dst_unused:UNUSED_PRESERVE src0_sel:WORD_1
	v_exp_f16_sdwa v239, v239 dst_sel:WORD_1 dst_unused:UNUSED_PRESERVE src0_sel:WORD_1
	v_pk_add_f16 v40, v38, v36
	v_pk_add_f16 v41, v39, v37
	v_pk_fma_f16 v238, v36, v238, v40 neg_lo:[1,0,0] neg_hi:[1,0,0]
	v_pk_fma_f16 v239, v37, v239, v41 neg_lo:[1,0,0] neg_hi:[1,0,0]
	v_cvt_pk_f16_f32 v38, v68, v69
	v_cvt_pk_f16_f32 v39, v70, v71
	v_and_b32 v36, s35, v38
	v_and_b32 v37, s35, v39
	v_pk_fma_f16 v240, v36, s42, v227
	v_pk_fma_f16 v241, v37, s42, v227
	v_pk_fma_f16 v240, v240, v36, s43
	v_pk_fma_f16 v241, v241, v37, s43
	v_cvt_pk_f16_f32 v243, v72, v73
	v_cvt_pk_f16_f32 v244, v74, v75
	v_and_b32 v209, s35, v243
	v_and_b32 v242, s35, v244
	v_pk_fma_f16 v68, v209, s42, v227
	v_pk_fma_f16 v69, v242, s42, v227
	v_pk_fma_f16 v68, v68, v209, s43
	v_pk_fma_f16 v69, v69, v242, s43
	v_cvt_pk_f16_f32 v74, v76, v77
	v_cvt_pk_f16_f32 v75, v78, v79
	v_and_b32 v72, s35, v74
	v_and_b32 v73, s35, v75
	v_pk_fma_f16 v70, v72, s42, v227
	v_pk_fma_f16 v71, v73, s42, v227
	v_pk_fma_f16 v70, v70, v72, s43
	v_pk_fma_f16 v71, v71, v73, s43
	s_cmp_eq_u32 s8, 0
	v_pk_mul_f16 v240, v240, v36
	v_pk_mul_f16 v241, v241, v37
	v_exp_f16_sdwa v240, v240 dst_sel:WORD_0 dst_unused:UNUSED_PRESERVE src0_sel:WORD_0
	v_exp_f16_sdwa v241, v241 dst_sel:WORD_0 dst_unused:UNUSED_PRESERVE src0_sel:WORD_0
	v_exp_f16_sdwa v240, v240 dst_sel:WORD_1 dst_unused:UNUSED_PRESERVE src0_sel:WORD_1
	v_exp_f16_sdwa v241, v241 dst_sel:WORD_1 dst_unused:UNUSED_PRESERVE src0_sel:WORD_1
	v_pk_add_f16 v40, v38, v36
	v_pk_add_f16 v41, v39, v37
	v_pk_fma_f16 v240, v36, v240, v40 neg_lo:[1,0,0] neg_hi:[1,0,0]
	v_pk_fma_f16 v241, v37, v241, v41 neg_lo:[1,0,0] neg_hi:[1,0,0]
	v_pk_mul_f16 v68, v68, v209
	v_pk_mul_f16 v69, v69, v242
	v_exp_f16_sdwa v68, v68 dst_sel:WORD_0 dst_unused:UNUSED_PRESERVE src0_sel:WORD_0
	v_exp_f16_sdwa v69, v69 dst_sel:WORD_0 dst_unused:UNUSED_PRESERVE src0_sel:WORD_0
	v_exp_f16_sdwa v68, v68 dst_sel:WORD_1 dst_unused:UNUSED_PRESERVE src0_sel:WORD_1
	v_exp_f16_sdwa v69, v69 dst_sel:WORD_1 dst_unused:UNUSED_PRESERVE src0_sel:WORD_1
	v_pk_add_f16 v76, v243, v209
	v_pk_add_f16 v77, v244, v242
	v_pk_fma_f16 v68, v209, v68, v76 neg_lo:[1,0,0] neg_hi:[1,0,0]
	v_pk_fma_f16 v69, v242, v69, v77 neg_lo:[1,0,0] neg_hi:[1,0,0]
	v_pk_mul_f16 v70, v70, v72
	v_pk_mul_f16 v71, v71, v73
	v_exp_f16_sdwa v70, v70 dst_sel:WORD_0 dst_unused:UNUSED_PRESERVE src0_sel:WORD_0
	v_exp_f16_sdwa v71, v71 dst_sel:WORD_0 dst_unused:UNUSED_PRESERVE src0_sel:WORD_0
	v_exp_f16_sdwa v70, v70 dst_sel:WORD_1 dst_unused:UNUSED_PRESERVE src0_sel:WORD_1
	v_exp_f16_sdwa v71, v71 dst_sel:WORD_1 dst_unused:UNUSED_PRESERVE src0_sel:WORD_1
	v_pk_add_f16 v76, v74, v72
	v_pk_add_f16 v77, v75, v73
	v_pk_fma_f16 v70, v72, v70, v76 neg_lo:[1,0,0] neg_hi:[1,0,0]
	v_pk_fma_f16 v71, v73, v71, v77 neg_lo:[1,0,0] neg_hi:[1,0,0]
	v_cvt_pk_f16_f32 v74, v48, v49
	v_cvt_pk_f16_f32 v75, v50, v51
	v_and_b32 v72, s35, v74
	v_and_b32 v73, s35, v75
	v_pk_fma_f16 v64, v72, s42, v227
	v_pk_fma_f16 v65, v73, s42, v227
	v_pk_fma_f16 v64, v64, v72, s43
	v_pk_fma_f16 v65, v65, v73, s43
	v_cvt_pk_f16_f32 v78, v52, v53
	v_cvt_pk_f16_f32 v79, v54, v55
	v_and_b32 v76, s35, v78
	v_and_b32 v77, s35, v79
	v_pk_fma_f16 v66, v76, s42, v227
	v_pk_fma_f16 v67, v77, s42, v227
	v_pk_fma_f16 v66, v66, v76, s43
	v_pk_fma_f16 v67, v67, v77, s43
	v_pk_mul_f16 v64, v64, v72
	v_pk_mul_f16 v65, v65, v73
	v_exp_f16_sdwa v64, v64 dst_sel:WORD_0 dst_unused:UNUSED_PRESERVE src0_sel:WORD_0
	v_exp_f16_sdwa v65, v65 dst_sel:WORD_0 dst_unused:UNUSED_PRESERVE src0_sel:WORD_0
	v_exp_f16_sdwa v64, v64 dst_sel:WORD_1 dst_unused:UNUSED_PRESERVE src0_sel:WORD_1
	v_exp_f16_sdwa v65, v65 dst_sel:WORD_1 dst_unused:UNUSED_PRESERVE src0_sel:WORD_1
	v_pk_add_f16 v209, v74, v72
	v_pk_add_f16 v242, v75, v73
	v_pk_fma_f16 v64, v72, v64, v209 neg_lo:[1,0,0] neg_hi:[1,0,0]
	v_pk_fma_f16 v65, v73, v65, v242 neg_lo:[1,0,0] neg_hi:[1,0,0]
	v_pk_mul_f16 v66, v66, v76
	v_pk_mul_f16 v67, v67, v77
	v_exp_f16_sdwa v66, v66 dst_sel:WORD_0 dst_unused:UNUSED_PRESERVE src0_sel:WORD_0
	v_exp_f16_sdwa v67, v67 dst_sel:WORD_0 dst_unused:UNUSED_PRESERVE src0_sel:WORD_0
	v_exp_f16_sdwa v66, v66 dst_sel:WORD_1 dst_unused:UNUSED_PRESERVE src0_sel:WORD_1
	v_exp_f16_sdwa v67, v67 dst_sel:WORD_1 dst_unused:UNUSED_PRESERVE src0_sel:WORD_1
	v_pk_add_f16 v72, v78, v76
	v_pk_add_f16 v73, v79, v77
	v_pk_fma_f16 v66, v76, v66, v72 neg_lo:[1,0,0] neg_hi:[1,0,0]
	v_pk_fma_f16 v67, v77, v67, v73 neg_lo:[1,0,0] neg_hi:[1,0,0]
	v_cvt_pk_f16_f32 v74, v56, v57
	v_cvt_pk_f16_f32 v75, v58, v59
	v_and_b32 v72, s35, v74
	v_and_b32 v73, s35, v75
	v_pk_fma_f16 v48, v72, s42, v227
	v_pk_fma_f16 v49, v73, s42, v227
	v_pk_fma_f16 v48, v48, v72, s43
	v_pk_fma_f16 v49, v49, v73, s43
	v_cvt_pk_f16_f32 v58, v60, v61
	v_cvt_pk_f16_f32 v59, v62, v63
	v_and_b32 v56, s35, v58
	v_and_b32 v57, s35, v59
	v_pk_fma_f16 v50, v56, s42, v227
	v_pk_fma_f16 v51, v57, s42, v227
	v_pk_fma_f16 v50, v50, v56, s43
	v_pk_fma_f16 v51, v51, v57, s43
	v_pk_mul_f16 v48, v48, v72
	v_pk_mul_f16 v49, v49, v73
	v_exp_f16_sdwa v48, v48 dst_sel:WORD_0 dst_unused:UNUSED_PRESERVE src0_sel:WORD_0
	v_exp_f16_sdwa v49, v49 dst_sel:WORD_0 dst_unused:UNUSED_PRESERVE src0_sel:WORD_0
	v_exp_f16_sdwa v48, v48 dst_sel:WORD_1 dst_unused:UNUSED_PRESERVE src0_sel:WORD_1
	v_exp_f16_sdwa v49, v49 dst_sel:WORD_1 dst_unused:UNUSED_PRESERVE src0_sel:WORD_1
	v_pk_add_f16 v62, v74, v72
	v_pk_add_f16 v63, v75, v73
	v_pk_fma_f16 v48, v72, v48, v62 neg_lo:[1,0,0] neg_hi:[1,0,0]
	v_pk_fma_f16 v49, v73, v49, v63 neg_lo:[1,0,0] neg_hi:[1,0,0]
	v_pk_mul_f16 v50, v50, v56
	v_pk_mul_f16 v51, v51, v57
	v_exp_f16_sdwa v50, v50 dst_sel:WORD_0 dst_unused:UNUSED_PRESERVE src0_sel:WORD_0
	v_exp_f16_sdwa v51, v51 dst_sel:WORD_0 dst_unused:UNUSED_PRESERVE src0_sel:WORD_0
	v_exp_f16_sdwa v50, v50 dst_sel:WORD_1 dst_unused:UNUSED_PRESERVE src0_sel:WORD_1
	v_exp_f16_sdwa v51, v51 dst_sel:WORD_1 dst_unused:UNUSED_PRESERVE src0_sel:WORD_1
	v_pk_add_f16 v62, v58, v56
	v_pk_add_f16 v63, v59, v57
	v_pk_fma_f16 v50, v56, v50, v62 neg_lo:[1,0,0] neg_hi:[1,0,0]
	v_pk_fma_f16 v51, v57, v51, v63 neg_lo:[1,0,0] neg_hi:[1,0,0]
	ds_write2_b64 v246, v[238:239], v[240:241] offset0:136 offset1:138
	ds_write2_b64 v246, v[64:65], v[66:67] offset0:144 offset1:146
	ds_write2_b64 v246, v[68:69], v[70:71] offset0:140 offset1:142
	ds_write2_b64 v246, v[48:49], v[50:51] offset0:148 offset1:150
	ds_read_b64 v[24:25], v249
	ds_read_b64 v[26:27], v249 offset:8
	ds_read_b64 v[28:29], v249 offset:64
	ds_read_b64 v[30:31], v249 offset:72
	ds_read_b64 v[40:41], v250
	ds_read_b64 v[42:43], v250 offset:8
	ds_read_b64 v[44:45], v250 offset:64
	ds_read_b64 v[46:47], v250 offset:72
	s_waitcnt lgkmcnt(4)
	v_mfma_f32_16x16x32_f16 v[32:35], v[24:27], v[16:19], 0
	v_mfma_f32_16x16x32_f16 v[32:35], v[28:31], v[20:23], v[32:35]
	s_waitcnt lgkmcnt(0)
	v_mfma_f32_16x16x32_f16 v[36:39], v[40:43], v[16:19], 0
	v_mfma_f32_16x16x32_f16 v[36:39], v[44:47], v[20:23], v[36:39]
	s_nop 7
	v_max3_f32 v52, v32, v33, v34
	v_max3_f32 v52, v52, v35, v36
	v_max3_f32 v52, v52, v37, v38
	v_max_f32_e32 v52, v52, v39
	v_mov_b32_e32 v53, v52
	s_nop 1
	v_permlane16_swap_b32_e32 v52, v53
	s_nop 0
	v_max_f32_e32 v52, v52, v53
	v_mov_b32_e32 v53, v52
	s_nop 1
	v_permlane32_swap_b32_e32 v52, v53
	s_nop 0
	v_max_f32_e32 v48, v52, v53
	s_cbranch_scc1 .LBB0_23
	v_add_f32_e32 v49, 0x41000000, v237
	v_cmp_gt_f32_e32 vcc, v48, v49
	s_cbranch_vccz .LBB0_24
	v_max_f32_e32 v48, v48, v48
	v_max_f32_e32 v49, v237, v237
	v_max_f32_e32 v49, v49, v48
	v_sub_f32_e32 v48, v237, v49
	v_exp_f32_e32 v48, v48
	v_mov_b32_e32 v237, v49
	v_pk_mul_f32 v[14:15], v[48:49], v[14:15] op_sel_hi:[0,1]
	v_pk_mul_f32 v[12:13], v[48:49], v[12:13] op_sel_hi:[0,1]
	v_pk_mul_f32 v[10:11], v[48:49], v[10:11] op_sel_hi:[0,1]
	v_pk_mul_f32 v[8:9], v[48:49], v[8:9] op_sel_hi:[0,1]
	v_pk_mul_f32 v[6:7], v[48:49], v[6:7] op_sel_hi:[0,1]
	v_pk_mul_f32 v[4:5], v[48:49], v[4:5] op_sel_hi:[0,1]
	v_pk_mul_f32 v[2:3], v[48:49], v[2:3] op_sel_hi:[0,1]
	v_pk_mul_f32 v[0:1], v[48:49], v[0:1] op_sel_hi:[0,1]
	v_mul_f32_e32 v236, v236, v48
	s_branch .LBB0_24
